# EpiDown: 4 gain + 8 gate loads issued together before the MFMA drain nops (one round trip instead of three)
# baseline (speedup 1.0000x reference)
; #define GAS __attribute__((address_space(1)))
;     ...
;         if constexpr (FP8) { asm volatile("s_nop 15\n\ts_nop 15\n\ts_nop 15\n\ts_nop 15" ::: "memory"); }
;     __device__ __forceinline__ void operator()(const f32x4 (&acc)[2][2][4][2], const Unit& u, int wr, int wc, int fr, int fq) const {
;         const int b = u.pm < 256 ? (u.pm & 15) : 16;
;         const float* g2 = modL + b * 6144 + 5 * 1024;
;         const int row0 = u.pm * BM + wr * 64 + fr, col0 = (u.pn & 3) * BM + wc * 32 + 8 * fq;
;         constexpr float ds = SC_Y / (SC_W * SC_HID);
;         f32x4 gv[2][2];
; #pragma unroll
;         for (int bj = 0; bj < 2; ++bj)
; #pragma unroll
;             for (int n = 0; n < 2; ++n) gv[bj][n] = *(const f32x4*)(g2 + col0 + bj * HALF + 4 * n) * ds;
;         float gts[2][4];
; #pragma unroll
;         for (int ai = 0; ai < 2; ++ai)
; #pragma unroll
;             for (int m = 0; m < 4; ++m) gts[ai][m] = ((const GAS float*)gate)[row0 + ai * HALF + m * 16];
; #pragma unroll
;         for (int ai = 0; ai < 2; ++ai)
; #pragma unroll
;             for (int m = 0; m < 4; ++m) { const int row = row0 + ai * HALF + m * 16; const float gt = gts[ai][m]; unsigned char* rowp = Y8 + (size_t)row * D + col0;
; #pragma unroll
;                 for (int bj = 0; bj < 2; ++bj) { const f32x4 v0 = acc[ai][bj][m][0] * (gv[bj][0] * gt), v1 = acc[ai][bj][m][1] * (gv[bj][1] * gt); u32x2 w;
;                     w.x = pack4_fp8(v0[0], v0[1], v0[2], v0[3]); w.y = pack4_fp8(v1[0], v1[1], v1[2], v1[3]);
;                     *(u32x2*)(rowp + bj * HALF) = w; } }
.LBB0_1502:
	s_and_b32 s2, s53, 15
	s_cmpk_lt_i32 s53, 0x100
	s_mulk_i32 s2, 0x1800
	s_cselect_b32 s2, s2, 0x18000
	s_lshl_b32 s2, s2, 2
	s_add_u32 s2, s46, s2
	s_addc_u32 s3, s47, 0
	s_lshl_b32 s6, s54, 8
	s_and_b32 s6, s6, 0x300
	v_or_b32_e32 v190, s6, v172
	v_lshlrev_b32_e32 v2, 2, v190
	v_mov_b32_e32 v3, v191
	v_lshl_add_u64 v[2:3], s[2:3], 0, v[2:3]
	s_mov_b64 s[2:3], 0x5000
	v_lshl_add_u64 v[22:23], v[2:3], 0, s[2:3]
	global_load_dwordx4 v[2:5], v[22:23], off
	global_load_dwordx4 v[6:9], v[22:23], off offset:16
	global_load_dwordx4 v[194:197], v[22:23], off offset:512
	global_load_dwordx4 v[198:201], v[22:23], off offset:528
	v_lshl_add_u32 v20, s53, 8, v1
	v_readlane_b32 s2, v252, 11
	v_ashrrev_i32_e32 v21, 31, v20
	v_readlane_b32 s3, v252, 12
	v_or_b32_e32 v170, 16, v20
	v_ashrrev_i32_e32 v171, 31, v170
	v_lshl_add_u64 v[18:19], v[20:21], 2, s[2:3]
	global_load_dword v174, v[18:19], off
	v_lshl_add_u64 v[22:23], v[170:171], 2, s[2:3]
	global_load_dword v168, v[22:23], off
	v_or_b32_e32 v166, 32, v20
	v_ashrrev_i32_e32 v167, 31, v166
	v_lshl_add_u64 v[22:23], v[166:167], 2, s[2:3]
	global_load_dword v32, v[22:23], off
	v_or_b32_e32 v30, 48, v20
	v_ashrrev_i32_e32 v31, 31, v30
	v_lshl_add_u64 v[22:23], v[30:31], 2, s[2:3]
	global_load_dword v28, v[22:23], off
	global_load_dword v26, v[18:19], off offset:512
	global_load_dword v24, v[18:19], off offset:576
	s_nop 0
	global_load_dword v22, v[18:19], off offset:640
	s_nop 0
	global_load_dword v18, v[18:19], off offset:704
	s_nop 15
	s_nop 15
	s_nop 15
	s_nop 15
	s_mov_b32 s2, 0x3d800000
	s_waitcnt vmcnt(0)
	v_pk_mul_f32 v[14:15], v[4:5], s[2:3] op_sel_hi:[1,0]
	v_pk_mul_f32 v[16:17], v[2:3], s[2:3] op_sel_hi:[1,0]
	v_pk_mul_f32 v[10:11], v[8:9], s[2:3] op_sel_hi:[1,0]
	v_pk_mul_f32 v[12:13], v[6:7], s[2:3] op_sel_hi:[1,0]
	v_pk_mul_f32 v[6:7], v[196:197], s[2:3] op_sel_hi:[1,0]
	v_pk_mul_f32 v[8:9], v[194:195], s[2:3] op_sel_hi:[1,0]
	v_pk_mul_f32 v[2:3], v[200:201], s[2:3] op_sel_hi:[1,0]
	v_pk_mul_f32 v[4:5], v[198:199], s[2:3] op_sel_hi:[1,0]
	v_lshlrev_b64 v[20:21], 10, v[20:21]
	v_lshl_add_u64 v[20:21], s[90:91], 0, v[20:21]
	v_lshl_add_u64 v[20:21], v[20:21], 0, v[190:191]
	v_lshlrev_b64 v[30:31], 10, v[30:31]
	v_lshl_add_u64 v[30:31], s[90:91], 0, v[30:31]
	v_lshl_add_u64 v[30:31], v[30:31], 0, v[190:191]
	s_mov_b64 s[2:3], 0x20000
	s_waitcnt vmcnt(7)
	v_pk_mul_f32 v[176:177], v[16:17], v[174:175] op_sel_hi:[1,0]
	s_nop 0
	v_pk_mul_f32 v[154:155], v[154:155], v[176:177]
	v_pk_mul_f32 v[178:179], v[14:15], v[174:175] op_sel_hi:[1,0]
	v_med3_f32 v19, v154, s15, v212
	v_med3_f32 v23, v155, s15, v212
	v_mov_b32_e32 v154, v191
	v_cvt_pk_fp8_f32 v154, v19, v23
	v_pk_mul_f32 v[156:157], v[156:157], v[178:179]
	v_pk_mul_f32 v[178:179], v[12:13], v[174:175] op_sel_hi:[1,0]
	v_med3_f32 v19, v156, s15, v212
	v_pk_mul_f32 v[158:159], v[158:159], v[178:179]
	v_med3_f32 v23, v157, s15, v212
	v_cvt_pk_fp8_f32 v154, v19, v23 op_sel:[0,0,1]
	v_med3_f32 v19, v158, s15, v212
	v_med3_f32 v23, v159, s15, v212
	v_mov_b32_e32 v155, v191
	v_cvt_pk_fp8_f32 v155, v19, v23
	v_pk_mul_f32 v[176:177], v[10:11], v[174:175] op_sel_hi:[1,0]
	v_pk_mul_f32 v[156:157], v[8:9], v[174:175] op_sel_hi:[1,0]
	v_pk_mul_f32 v[160:161], v[160:161], v[176:177]
	v_pk_mul_f32 v[146:147], v[146:147], v[156:157]
	v_med3_f32 v19, v160, s15, v212
	v_med3_f32 v23, v161, s15, v212
	v_cvt_pk_fp8_f32 v155, v19, v23 op_sel:[0,0,1]
	v_med3_f32 v19, v146, s15, v212
	v_med3_f32 v23, v147, s15, v212
	v_mov_b32_e32 v146, v191
	v_cvt_pk_fp8_f32 v146, v19, v23
	global_store_dwordx2 v[20:21], v[154:155], off
	v_pk_mul_f32 v[154:155], v[6:7], v[174:175] op_sel_hi:[1,0]
	v_pk_mul_f32 v[156:157], v[4:5], v[174:175] op_sel_hi:[1,0]
	v_pk_mul_f32 v[148:149], v[148:149], v[154:155]
	v_pk_mul_f32 v[150:151], v[150:151], v[156:157]
	v_med3_f32 v19, v148, s15, v212
	v_med3_f32 v23, v149, s15, v212
	v_cvt_pk_fp8_f32 v146, v19, v23 op_sel:[0,0,1]
	v_med3_f32 v19, v150, s15, v212
	v_med3_f32 v23, v151, s15, v212
	v_mov_b32_e32 v147, v191
	v_cvt_pk_fp8_f32 v147, v19, v23
	v_pk_mul_f32 v[154:155], v[2:3], v[174:175] op_sel_hi:[1,0]
	s_waitcnt vmcnt(7)
	v_pk_mul_f32 v[148:149], v[16:17], v[168:169] op_sel_hi:[1,0]
	v_pk_mul_f32 v[152:153], v[152:153], v[154:155]
	v_pk_mul_f32 v[138:139], v[138:139], v[148:149]
	v_med3_f32 v19, v152, s15, v212
	v_med3_f32 v23, v153, s15, v212
	v_cvt_pk_fp8_f32 v147, v19, v23 op_sel:[0,0,1]
	v_med3_f32 v19, v138, s15, v212
	v_med3_f32 v23, v139, s15, v212
	v_mov_b32_e32 v138, v191
	v_cvt_pk_fp8_f32 v138, v19, v23
	v_pk_mul_f32 v[150:151], v[14:15], v[168:169] op_sel_hi:[1,0]
	v_mov_b32_e32 v139, v191
	v_pk_mul_f32 v[140:141], v[140:141], v[150:151]
	v_pk_mul_f32 v[150:151], v[12:13], v[168:169] op_sel_hi:[1,0]
	v_med3_f32 v19, v140, s15, v212
	v_pk_mul_f32 v[130:131], v[130:131], v[150:151]
	v_med3_f32 v23, v141, s15, v212
	v_cvt_pk_fp8_f32 v138, v19, v23 op_sel:[0,0,1]
	v_med3_f32 v19, v130, s15, v212
	v_med3_f32 v23, v131, s15, v212
	v_pk_mul_f32 v[148:149], v[10:11], v[168:169] op_sel_hi:[1,0]
	v_cvt_pk_fp8_f32 v139, v19, v23
	v_pk_mul_f32 v[132:133], v[132:133], v[148:149]
	v_pk_mul_f32 v[130:131], v[6:7], v[168:169] op_sel_hi:[1,0]
	v_med3_f32 v19, v132, s15, v212
	v_med3_f32 v23, v133, s15, v212
	v_pk_mul_f32 v[132:133], v[8:9], v[168:169] op_sel_hi:[1,0]
	v_cvt_pk_fp8_f32 v139, v19, v23 op_sel:[0,0,1]
	v_pk_mul_f32 v[132:133], v[142:143], v[132:133]
	v_pk_mul_f32 v[130:131], v[144:145], v[130:131]
	v_med3_f32 v19, v132, s15, v212
	v_med3_f32 v23, v133, s15, v212
	v_mov_b32_e32 v132, v191
	v_cvt_pk_fp8_f32 v132, v19, v23
	v_pk_mul_f32 v[140:141], v[4:5], v[168:169] op_sel_hi:[1,0]
	global_store_dwordx2 v[20:21], v[146:147], off offset:128
	v_lshlrev_b64 v[146:147], 10, v[170:171]
	v_pk_mul_f32 v[134:135], v[134:135], v[140:141]
	v_med3_f32 v19, v130, s15, v212
	v_med3_f32 v23, v131, s15, v212
	v_lshl_add_u64 v[146:147], s[90:91], 0, v[146:147]
	v_cvt_pk_fp8_f32 v132, v19, v23 op_sel:[0,0,1]
	v_med3_f32 v19, v134, s15, v212
	v_med3_f32 v23, v135, s15, v212
	v_mov_b32_e32 v133, v191
	v_lshl_add_u64 v[146:147], v[146:147], 0, v[190:191]
	v_cvt_pk_fp8_f32 v133, v19, v23
	global_store_dwordx2 v[146:147], v[138:139], off
	v_pk_mul_f32 v[138:139], v[2:3], v[168:169] op_sel_hi:[1,0]
	s_waitcnt vmcnt(8)
;     __device__ __forceinline__ void operator()(const f32x4 (&acc)[2][2][4][2], const Unit& u, int wr, int wc, int fr, int fq) const {
;     ...
;         for (int ai = 0; ai < 2; ++ai)
; #pragma unroll
;             for (int m = 0; m < 4; ++m) { const int row = row0 + ai * HALF + m * 16; const float gt = gts[ai][m]; unsigned char* rowp = Y8 + (size_t)row * D + col0;
; #pragma unroll
;                 for (int bj = 0; bj < 2; ++bj) { const f32x4 v0 = acc[ai][bj][m][0] * (gv[bj][0] * gt), v1 = acc[ai][bj][m][1] * (gv[bj][1] * gt); u32x2 w;
;                     w.x = pack4_fp8(v0[0], v0[1], v0[2], v0[3]); w.y = pack4_fp8(v1[0], v1[1], v1[2], v1[3]);
;                     *(u32x2*)(rowp + bj * HALF) = w; } }
	v_pk_mul_f32 v[134:135], v[14:15], v[32:33] op_sel_hi:[1,0]
	v_pk_mul_f32 v[136:137], v[136:137], v[138:139]
	v_pk_mul_f32 v[128:129], v[128:129], v[134:135]
	v_med3_f32 v19, v136, s15, v212
	v_med3_f32 v23, v137, s15, v212
	v_cvt_pk_fp8_f32 v133, v19, v23 op_sel:[0,0,1]
	v_pk_mul_f32 v[134:135], v[12:13], v[32:33] op_sel_hi:[1,0]
	v_lshlrev_b64 v[130:131], 10, v[166:167]
	v_pk_mul_f32 v[122:123], v[122:123], v[134:135]
	global_store_dwordx2 v[146:147], v[132:133], off offset:128
	v_pk_mul_f32 v[132:133], v[16:17], v[32:33] op_sel_hi:[1,0]
	v_lshl_add_u64 v[130:131], s[90:91], 0, v[130:131]
	v_pk_mul_f32 v[126:127], v[126:127], v[132:133]
	v_pk_mul_f32 v[132:133], v[10:11], v[32:33] op_sel_hi:[1,0]
	v_med3_f32 v19, v126, s15, v212
	v_med3_f32 v23, v127, s15, v212
	v_mov_b32_e32 v126, v191
	v_cvt_pk_fp8_f32 v126, v19, v23
	v_med3_f32 v19, v128, s15, v212
	v_med3_f32 v23, v129, s15, v212
	v_mov_b32_e32 v127, v191
	v_cvt_pk_fp8_f32 v126, v19, v23 op_sel:[0,0,1]
	v_med3_f32 v19, v122, s15, v212
	v_med3_f32 v23, v123, s15, v212
	v_cvt_pk_fp8_f32 v127, v19, v23
	v_pk_mul_f32 v[124:125], v[124:125], v[132:133]
	v_pk_mul_f32 v[122:123], v[6:7], v[32:33] op_sel_hi:[1,0]
	v_med3_f32 v19, v124, s15, v212
	v_med3_f32 v23, v125, s15, v212
	v_pk_mul_f32 v[124:125], v[8:9], v[32:33] op_sel_hi:[1,0]
	v_pk_mul_f32 v[120:121], v[120:121], v[122:123]
	v_pk_mul_f32 v[118:119], v[118:119], v[124:125]
	v_pk_mul_f32 v[122:123], v[2:3], v[32:33] op_sel_hi:[1,0]
	v_pk_mul_f32 v[32:33], v[4:5], v[32:33] op_sel_hi:[1,0]
	v_cvt_pk_fp8_f32 v127, v19, v23 op_sel:[0,0,1]
	v_pk_mul_f32 v[32:33], v[114:115], v[32:33]
	v_med3_f32 v19, v118, s15, v212
	v_med3_f32 v23, v119, s15, v212
	v_mov_b32_e32 v114, v191
	v_cvt_pk_fp8_f32 v114, v19, v23
	v_med3_f32 v19, v120, s15, v212
	v_med3_f32 v23, v121, s15, v212
	v_mov_b32_e32 v115, v191
	v_cvt_pk_fp8_f32 v114, v19, v23 op_sel:[0,0,1]
	v_med3_f32 v19, v32, s15, v212
	v_med3_f32 v23, v33, s15, v212
	v_cvt_pk_fp8_f32 v115, v19, v23
	v_pk_mul_f32 v[116:117], v[116:117], v[122:123]
	s_waitcnt vmcnt(8)
	v_pk_mul_f32 v[32:33], v[16:17], v[28:29] op_sel_hi:[1,0]
	v_med3_f32 v19, v116, s15, v212
	v_med3_f32 v23, v117, s15, v212
	v_cvt_pk_fp8_f32 v115, v19, v23 op_sel:[0,0,1]
	v_pk_mul_f32 v[32:33], v[110:111], v[32:33]
	v_lshl_add_u64 v[130:131], v[130:131], 0, v[190:191]
	v_med3_f32 v19, v32, s15, v212
	v_med3_f32 v23, v33, s15, v212
	v_mov_b32_e32 v32, v191
	v_cvt_pk_fp8_f32 v32, v19, v23
	global_store_dwordx2 v[130:131], v[114:115], off offset:128
	v_pk_mul_f32 v[114:115], v[14:15], v[28:29] op_sel_hi:[1,0]
	v_mov_b32_e32 v33, v191
	v_pk_mul_f32 v[112:113], v[112:113], v[114:115]
	v_pk_mul_f32 v[114:115], v[12:13], v[28:29] op_sel_hi:[1,0]
	v_med3_f32 v19, v112, s15, v212
	v_pk_mul_f32 v[106:107], v[106:107], v[114:115]
	v_med3_f32 v23, v113, s15, v212
	v_cvt_pk_fp8_f32 v32, v19, v23 op_sel:[0,0,1]
	v_med3_f32 v19, v106, s15, v212
	v_med3_f32 v23, v107, s15, v212
	v_cvt_pk_fp8_f32 v33, v19, v23
	v_pk_mul_f32 v[110:111], v[10:11], v[28:29] op_sel_hi:[1,0]
	v_pk_mul_f32 v[106:107], v[8:9], v[28:29] op_sel_hi:[1,0]
	v_pk_mul_f32 v[108:109], v[108:109], v[110:111]
	v_pk_mul_f32 v[94:95], v[94:95], v[106:107]
	v_med3_f32 v19, v108, s15, v212
	v_med3_f32 v23, v109, s15, v212
	v_cvt_pk_fp8_f32 v33, v19, v23 op_sel:[0,0,1]
	v_med3_f32 v19, v94, s15, v212
	v_med3_f32 v23, v95, s15, v212
	global_store_dwordx2 v[130:131], v[126:127], off
	global_store_dwordx2 v[30:31], v[32:33], off
	v_pk_mul_f32 v[32:33], v[6:7], v[28:29] op_sel_hi:[1,0]
	s_nop 0
	v_pk_mul_f32 v[32:33], v[96:97], v[32:33]
	v_pk_mul_f32 v[96:97], v[2:3], v[28:29] op_sel_hi:[1,0]
	v_pk_mul_f32 v[28:29], v[4:5], v[28:29] op_sel_hi:[1,0]
	v_pk_mul_f32 v[92:93], v[92:93], v[96:97]
	v_pk_mul_f32 v[28:29], v[90:91], v[28:29]
	v_mov_b32_e32 v90, v191
	v_cvt_pk_fp8_f32 v90, v19, v23
	v_med3_f32 v19, v32, s15, v212
	v_med3_f32 v23, v33, s15, v212
	v_mov_b32_e32 v91, v191
	v_cvt_pk_fp8_f32 v90, v19, v23 op_sel:[0,0,1]
	v_med3_f32 v19, v28, s15, v212
	v_med3_f32 v23, v29, s15, v212
	v_cvt_pk_fp8_f32 v91, v19, v23
	v_med3_f32 v19, v92, s15, v212
	v_med3_f32 v23, v93, s15, v212
	s_waitcnt vmcnt(10)
	v_pk_mul_f32 v[32:33], v[14:15], v[26:27] op_sel_hi:[1,0]
	v_cvt_pk_fp8_f32 v91, v19, v23 op_sel:[0,0,1]
	v_pk_mul_f32 v[32:33], v[104:105], v[32:33]
	v_pk_mul_f32 v[92:93], v[12:13], v[26:27] op_sel_hi:[1,0]
	v_lshl_add_u64 v[28:29], v[20:21], 0, s[2:3]
	global_store_dwordx2 v[30:31], v[90:91], off offset:128
	v_pk_mul_f32 v[30:31], v[16:17], v[26:27] op_sel_hi:[1,0]
	v_pk_mul_f32 v[92:93], v[98:99], v[92:93]
	v_pk_mul_f32 v[30:31], v[102:103], v[30:31]
	v_pk_mul_f32 v[90:91], v[10:11], v[26:27] op_sel_hi:[1,0]
	v_med3_f32 v19, v30, s15, v212
	v_med3_f32 v23, v31, s15, v212
	v_mov_b32_e32 v30, v191
	v_cvt_pk_fp8_f32 v30, v19, v23
	v_med3_f32 v19, v32, s15, v212
	v_med3_f32 v23, v33, s15, v212
	v_mov_b32_e32 v31, v191
	v_cvt_pk_fp8_f32 v30, v19, v23 op_sel:[0,0,1]
	v_med3_f32 v19, v92, s15, v212
	v_med3_f32 v23, v93, s15, v212
	v_cvt_pk_fp8_f32 v31, v19, v23
	v_pk_mul_f32 v[90:91], v[100:101], v[90:91]
	s_mov_b32 s2, 0x20000
	v_med3_f32 v19, v90, s15, v212
	v_med3_f32 v23, v91, s15, v212
	v_cvt_pk_fp8_f32 v31, v19, v23 op_sel:[0,0,1]
	v_add_co_u32_e32 v32, vcc, s2, v20
	s_mov_b64 s[2:3], 0x24000
	s_nop 0
	v_addc_co_u32_e32 v33, vcc, 0, v21, vcc
	global_store_dwordx2 v[32:33], v[30:31], off
	v_pk_mul_f32 v[32:33], v[8:9], v[26:27] op_sel_hi:[1,0]
	v_pk_mul_f32 v[30:31], v[6:7], v[26:27] op_sel_hi:[1,0]
	v_pk_mul_f32 v[32:33], v[86:87], v[32:33]
	v_pk_mul_f32 v[30:31], v[88:89], v[30:31]
	v_med3_f32 v19, v32, s15, v212
	v_med3_f32 v23, v33, s15, v212
	v_mov_b32_e32 v32, v191
	v_cvt_pk_fp8_f32 v32, v19, v23
	v_pk_mul_f32 v[86:87], v[2:3], v[26:27] op_sel_hi:[1,0]
	v_pk_mul_f32 v[26:27], v[4:5], v[26:27] op_sel_hi:[1,0]
	v_med3_f32 v19, v30, s15, v212
	v_pk_mul_f32 v[26:27], v[82:83], v[26:27]
	v_med3_f32 v23, v31, s15, v212
	v_cvt_pk_fp8_f32 v32, v19, v23 op_sel:[0,0,1]
	v_med3_f32 v19, v26, s15, v212
	v_med3_f32 v23, v27, s15, v212
	v_mov_b32_e32 v33, v191
	v_cvt_pk_fp8_f32 v33, v19, v23
	v_pk_mul_f32 v[84:85], v[84:85], v[86:87]
	s_waitcnt vmcnt(11)
; #define PG8_BAR __builtin_amdgcn_s_barrier()
;     ...
;         if (!has_next) break;
;         cur = nxt; cA = nA; cB = nB; ++ui;
; #pragma unroll
;         for (int _h = 0; _h < 2; ++_h)
; #pragma unroll
;             for (int _i = 0; _i < 2; ++_i) cvo[_h][_i] = nvo[_h][_i];
;         if constexpr (ALIGN_EPI) { if (wr == 1) PG8_BAR; }
;     __device__ __forceinline__ void operator()(const f32x4 (&acc)[2][2][4][2], const Unit& u, int wr, int wc, int fr, int fq) const {
;     ...
;         for (int ai = 0; ai < 2; ++ai)
; #pragma unroll
;             for (int m = 0; m < 4; ++m) { const int row = row0 + ai * HALF + m * 16; const float gt = gts[ai][m]; unsigned char* rowp = Y8 + (size_t)row * D + col0;
; #pragma unroll
;                 for (int bj = 0; bj < 2; ++bj) { const f32x4 v0 = acc[ai][bj][m][0] * (gv[bj][0] * gt), v1 = acc[ai][bj][m][1] * (gv[bj][1] * gt); u32x2 w;
;                     w.x = pack4_fp8(v0[0], v0[1], v0[2], v0[3]); w.y = pack4_fp8(v1[0], v1[1], v1[2], v1[3]);
;                     *(u32x2*)(rowp + bj * HALF) = w; } }
	v_pk_mul_f32 v[30:31], v[14:15], v[24:25] op_sel_hi:[1,0]
	v_med3_f32 v19, v84, s15, v212
	v_med3_f32 v23, v85, s15, v212
	v_cvt_pk_fp8_f32 v33, v19, v23 op_sel:[0,0,1]
	v_pk_mul_f32 v[30:31], v[80:81], v[30:31]
	v_lshl_add_u64 v[26:27], v[20:21], 0, s[2:3]
	s_mov_b32 s2, 0x24000
	global_store_dwordx2 v[28:29], v[32:33], off offset:128
	v_pk_mul_f32 v[28:29], v[16:17], v[24:25] op_sel_hi:[1,0]
	v_pk_mul_f32 v[32:33], v[10:11], v[24:25] op_sel_hi:[1,0]
	v_pk_mul_f32 v[28:29], v[78:79], v[28:29]
	v_pk_mul_f32 v[78:79], v[12:13], v[24:25] op_sel_hi:[1,0]
	v_med3_f32 v19, v28, s15, v212
	v_med3_f32 v23, v29, s15, v212
	v_mov_b32_e32 v28, v191
	v_cvt_pk_fp8_f32 v28, v19, v23
	v_pk_mul_f32 v[74:75], v[74:75], v[78:79]
	v_med3_f32 v19, v30, s15, v212
	v_med3_f32 v23, v31, s15, v212
	v_cvt_pk_fp8_f32 v28, v19, v23 op_sel:[0,0,1]
	v_med3_f32 v19, v74, s15, v212
	v_med3_f32 v23, v75, s15, v212
	v_mov_b32_e32 v29, v191
	v_cvt_pk_fp8_f32 v29, v19, v23
	v_pk_mul_f32 v[32:33], v[76:77], v[32:33]
	v_add_co_u32_e32 v30, vcc, s2, v20
	v_med3_f32 v19, v32, s15, v212
	v_med3_f32 v23, v33, s15, v212
	v_cvt_pk_fp8_f32 v29, v19, v23 op_sel:[0,0,1]
	v_addc_co_u32_e32 v31, vcc, 0, v21, vcc
	v_pk_mul_f32 v[32:33], v[2:3], v[24:25] op_sel_hi:[1,0]
	global_store_dwordx2 v[30:31], v[28:29], off
	v_pk_mul_f32 v[30:31], v[8:9], v[24:25] op_sel_hi:[1,0]
	v_pk_mul_f32 v[28:29], v[6:7], v[24:25] op_sel_hi:[1,0]
	v_pk_mul_f32 v[30:31], v[70:71], v[30:31]
	v_pk_mul_f32 v[28:29], v[72:73], v[28:29]
	v_med3_f32 v19, v30, s15, v212
	v_med3_f32 v23, v31, s15, v212
	v_mov_b32_e32 v30, v191
	v_cvt_pk_fp8_f32 v30, v19, v23
	v_pk_mul_f32 v[24:25], v[4:5], v[24:25] op_sel_hi:[1,0]
	v_med3_f32 v19, v28, s15, v212
	v_pk_mul_f32 v[24:25], v[66:67], v[24:25]
	v_med3_f32 v23, v29, s15, v212
	v_cvt_pk_fp8_f32 v30, v19, v23 op_sel:[0,0,1]
	v_med3_f32 v19, v24, s15, v212
	v_med3_f32 v23, v25, s15, v212
	v_mov_b32_e32 v31, v191
	v_cvt_pk_fp8_f32 v31, v19, v23
	v_pk_mul_f32 v[32:33], v[68:69], v[32:33]
	s_mov_b64 s[2:3], 0x28000
	v_med3_f32 v19, v32, s15, v212
	v_med3_f32 v23, v33, s15, v212
	v_cvt_pk_fp8_f32 v31, v19, v23 op_sel:[0,0,1]
	s_waitcnt vmcnt(12)
	v_pk_mul_f32 v[28:29], v[14:15], v[22:23] op_sel_hi:[1,0]
	v_pk_mul_f32 v[32:33], v[12:13], v[22:23] op_sel_hi:[1,0]
	v_pk_mul_f32 v[28:29], v[64:65], v[28:29]
	global_store_dwordx2 v[26:27], v[30:31], off offset:128
	v_pk_mul_f32 v[26:27], v[16:17], v[22:23] op_sel_hi:[1,0]
	v_pk_mul_f32 v[30:31], v[10:11], v[22:23] op_sel_hi:[1,0]
	v_pk_mul_f32 v[26:27], v[62:63], v[26:27]
	v_pk_mul_f32 v[32:33], v[58:59], v[32:33]
	v_med3_f32 v19, v26, s15, v212
	v_med3_f32 v23, v27, s15, v212
	v_mov_b32_e32 v26, v191
	v_cvt_pk_fp8_f32 v26, v19, v23
	v_med3_f32 v19, v28, s15, v212
	v_med3_f32 v23, v29, s15, v212
	v_mov_b32_e32 v27, v191
	v_cvt_pk_fp8_f32 v26, v19, v23 op_sel:[0,0,1]
	v_med3_f32 v19, v32, s15, v212
	v_med3_f32 v23, v33, s15, v212
	v_cvt_pk_fp8_f32 v27, v19, v23
	v_pk_mul_f32 v[30:31], v[60:61], v[30:31]
	v_lshl_add_u64 v[24:25], v[20:21], 0, s[2:3]
	v_med3_f32 v19, v30, s15, v212
	v_med3_f32 v23, v31, s15, v212
	v_cvt_pk_fp8_f32 v27, v19, v23 op_sel:[0,0,1]
	s_mov_b32 s2, 0x28000
	v_add_co_u32_e32 v28, vcc, s2, v20
	v_pk_mul_f32 v[30:31], v[2:3], v[22:23] op_sel_hi:[1,0]
	s_nop 0
	v_addc_co_u32_e32 v29, vcc, 0, v21, vcc
	global_store_dwordx2 v[28:29], v[26:27], off
	v_pk_mul_f32 v[28:29], v[8:9], v[22:23] op_sel_hi:[1,0]
	v_pk_mul_f32 v[26:27], v[6:7], v[22:23] op_sel_hi:[1,0]
	v_pk_mul_f32 v[28:29], v[54:55], v[28:29]
	v_pk_mul_f32 v[26:27], v[56:57], v[26:27]
	v_med3_f32 v19, v28, s15, v212
	v_med3_f32 v29, v29, s15, v212
	v_mov_b32_e32 v28, v191
	v_cvt_pk_fp8_f32 v28, v19, v29
	v_pk_mul_f32 v[22:23], v[4:5], v[22:23] op_sel_hi:[1,0]
	v_med3_f32 v19, v26, s15, v212
	v_pk_mul_f32 v[22:23], v[50:51], v[22:23]
	v_med3_f32 v26, v27, s15, v212
	v_cvt_pk_fp8_f32 v28, v19, v26 op_sel:[0,0,1]
	v_med3_f32 v19, v22, s15, v212
	v_med3_f32 v22, v23, s15, v212
	v_mov_b32_e32 v29, v191
	v_pk_mul_f32 v[30:31], v[52:53], v[30:31]
	v_cvt_pk_fp8_f32 v29, v19, v22
	v_med3_f32 v19, v30, s15, v212
	s_waitcnt vmcnt(13)
	v_pk_mul_f32 v[16:17], v[16:17], v[18:19] op_sel_hi:[1,0]
	v_med3_f32 v22, v31, s15, v212
	v_pk_mul_f32 v[16:17], v[46:47], v[16:17]
	v_pk_mul_f32 v[12:13], v[12:13], v[18:19] op_sel_hi:[1,0]
	v_cvt_pk_fp8_f32 v29, v19, v22 op_sel:[0,0,1]
	v_pk_mul_f32 v[14:15], v[14:15], v[18:19] op_sel_hi:[1,0]
	v_pk_mul_f32 v[10:11], v[10:11], v[18:19] op_sel_hi:[1,0]
	v_pk_mul_f32 v[12:13], v[42:43], v[12:13]
	v_med3_f32 v19, v16, s15, v212
	v_med3_f32 v17, v17, s15, v212
	v_mov_b32_e32 v16, v191
	v_cvt_pk_fp8_f32 v16, v19, v17
	v_med3_f32 v12, v12, s15, v212
	v_med3_f32 v13, v13, s15, v212
	v_mov_b32_e32 v17, v191
	v_cvt_pk_fp8_f32 v17, v12, v13
	v_pk_mul_f32 v[14:15], v[48:49], v[14:15]
	v_pk_mul_f32 v[10:11], v[44:45], v[10:11]
	v_med3_f32 v14, v14, s15, v212
	v_med3_f32 v15, v15, s15, v212
	v_med3_f32 v10, v10, s15, v212
	v_med3_f32 v11, v11, s15, v212
	s_mov_b64 s[2:3], 0x2c000
	v_cvt_pk_fp8_f32 v16, v14, v15 op_sel:[0,0,1]
	v_cvt_pk_fp8_f32 v17, v10, v11 op_sel:[0,0,1]
	v_lshl_add_u64 v[22:23], v[20:21], 0, s[2:3]
	s_mov_b32 s2, 0x2c000
	v_add_co_u32_e32 v10, vcc, s2, v20
	v_pk_mul_f32 v[8:9], v[8:9], v[18:19] op_sel_hi:[1,0]
	s_nop 0
	v_addc_co_u32_e32 v11, vcc, 0, v21, vcc
	v_pk_mul_f32 v[8:9], v[38:39], v[8:9]
	v_pk_mul_f32 v[4:5], v[4:5], v[18:19] op_sel_hi:[1,0]
	global_store_dwordx2 v[10:11], v[16:17], off
	v_pk_mul_f32 v[4:5], v[34:35], v[4:5]
	v_med3_f32 v10, v8, s15, v212
	v_med3_f32 v9, v9, s15, v212
	v_mov_b32_e32 v8, v191
	v_cvt_pk_fp8_f32 v8, v10, v9
	v_med3_f32 v4, v4, s15, v212
	v_med3_f32 v5, v5, s15, v212
	v_mov_b32_e32 v9, v191
	v_cvt_pk_fp8_f32 v9, v4, v5
	v_pk_mul_f32 v[6:7], v[6:7], v[18:19] op_sel_hi:[1,0]
	v_pk_mul_f32 v[2:3], v[2:3], v[18:19] op_sel_hi:[1,0]
	v_pk_mul_f32 v[6:7], v[40:41], v[6:7]
	v_pk_mul_f32 v[2:3], v[36:37], v[2:3]
	v_med3_f32 v6, v6, s15, v212
	v_med3_f32 v7, v7, s15, v212
	v_med3_f32 v2, v2, s15, v212
	v_med3_f32 v3, v3, s15, v212
	v_cvt_pk_fp8_f32 v8, v6, v7 op_sel:[0,0,1]
	v_cvt_pk_fp8_f32 v9, v2, v3 op_sel:[0,0,1]
	s_mov_b64 s[2:3], -1
	s_andn2_b64 vcc, exec, s[22:23]
	global_store_dwordx2 v[24:25], v[28:29], off offset:128
	global_store_dwordx2 v[22:23], v[8:9], off offset:128
	s_cbranch_vccnz .LBB0_1491
	s_andn2_b64 vcc, exec, s[0:1]
	s_cbranch_vccnz .LBB0_1490
	s_barrier
	s_branch .LBB0_1490
